# baseline (speedup 1.0000x reference)
.LBB0_21:
	v_exp_f32_e64 v156, -|v154|
	v_max_f32 v157, 0, v154
	v_add_f32 v156, 1.0, v156
	v_log_f32 v156, v156
	s_nop 0
	v_fma_mixlo_f16 v155, v156, 1.0, v157
	ds_write_b16 v148, v155
	v_mov_b32_e32 v192, v106
	v_mov_b32_e32 v193, v110
	v_mul_f32 v182, -2.0, v153
	s_nop 6
	ds_read_b128 v[208:211], v139
	s_waitcnt lgkmcnt(1)
	s_barrier
	ds_read_b128 v[212:215], v140
	s_waitcnt lgkmcnt(1)
	v_smfmac_f32_16x16x64_f16 v[192:195], v[208:211], v[6:13], v191
	ds_read_b128 v[216:219], v141
	s_waitcnt lgkmcnt(1)
	v_smfmac_f32_16x16x64_f16 v[192:195], v[212:215], v[14:21], v191
	ds_read_b128 v[220:223], v142
	s_waitcnt lgkmcnt(1)
	v_smfmac_f32_16x16x64_f16 v[192:195], v[216:219], v[26:33], v191
	s_waitcnt lgkmcnt(0)
	v_smfmac_f32_16x16x64_f16 v[192:195], v[220:223], v[34:41], v191
	s_nop 7
	v_cndmask_b32_e64 v154, v192, v193, s[0:1]
	v_exp_f32_e64 v156, -|v154|
	v_max_f32 v157, 0, v154
	v_add_f32 v156, 1.0, v156
	v_log_f32 v156, v156
	s_nop 0
	v_fma_mixlo_f16 v155, v156, 1.0, v157
	ds_write_b16 v149, v155
	v_mov_b32_e32 v200, v114
	v_mov_b32_e32 v201, v118
	v_mov_b32_e32 v204, v122
	v_mov_b32_e32 v205, v126
	s_nop 1
	ds_read_b128 v[208:211], v143
	s_waitcnt lgkmcnt(1)
	s_barrier
	ds_read_b128 v[212:215], v144
	s_waitcnt lgkmcnt(1)
	v_smfmac_f32_16x16x64_f16 v[200:203], v[208:211], v[42:49], v191
	ds_read_b128 v[216:219], v145
	v_smfmac_f32_16x16x64_f16 v[204:207], v[208:211], v[74:81], v191
	ds_read_b128 v[220:223], v146
	s_waitcnt lgkmcnt(2)
	v_smfmac_f32_16x16x64_f16 v[200:203], v[212:215], v[50:57], v191
	v_smfmac_f32_16x16x64_f16 v[204:207], v[212:215], v[82:89], v191
	s_waitcnt lgkmcnt(1)
	v_smfmac_f32_16x16x64_f16 v[200:203], v[216:219], v[58:65], v191
	v_smfmac_f32_16x16x64_f16 v[204:207], v[216:219], v[90:97], v191
	s_waitcnt lgkmcnt(0)
	v_smfmac_f32_16x16x64_f16 v[200:203], v[220:223], v[66:73], v191
	v_smfmac_f32_16x16x64_f16 v[204:207], v[220:223], v[98:105], v191
	s_nop 6
	v_cndmask_b32_e64 v170, v201, v200, s[6:7]
	v_cndmask_b32_e64 v170, v170, v204, s[0:1]
	v_cndmask_b32_e64 v170, v170, v205, s[4:5]
	v_exp_f32_e32 v170, v170
	s_nop 0
	v_add_f32_e32 v170, 1.0, v170
	v_rcp_f32_e32 v170, v170
	s_nop 0
	v_fmac_f32_e32 v153, v170, v182
	s_nop 1
	v_add_f32_dpp v153, v153, v153 quad_perm:[1,0,3,2] row_mask:0xf bank_mask:0xf bound_ctrl:1
	s_nop 1
	v_add_f32_dpp v153, v153, v153 quad_perm:[2,3,0,1] row_mask:0xf bank_mask:0xf bound_ctrl:1
	s_nop 1
	v_add_f32_dpp v153, v153, v153 row_half_mirror row_mask:0xf bank_mask:0xf bound_ctrl:1
	v_cvt_f16_f32_e32 v170, v153
	ds_write_b16 v150, v170
	s_waitcnt lgkmcnt(0)
	s_barrier
	ds_read_b128 v[154:157], v147
	s_waitcnt lgkmcnt(0)
	v_smfmac_f32_16x16x64_f16 v[130:133], v[154:157], v[248:255], v191
	s_nop 2
	v_add_u32_e32 v134, s3, v151
	ds_read_b32 v135, v134
	s_nop 2
	v_cndmask_b32_e64 v136, v130, v131, s[0:1]
	v_exp_f32_e64 v158, -|v136|
	v_max_f32 v159, 0, v136
	v_add_f32 v158, 1.0, v158
	v_log_f32 v158, v158
	s_nop 0
	v_fma_mixlo_f16 v137, v158, 1.0, v159
	ds_write_b16 v148, v137
	v_mov_b32_e32 v192, v106
	v_mov_b32_e32 v193, v110
	v_add_f32_e32 v136, v152, v153
	v_mul_f32 v137, -2.0, v135
	s_nop 6
	ds_read_b128 v[208:211], v139
	s_waitcnt lgkmcnt(1)
	s_barrier
	ds_read_b128 v[212:215], v140
	s_waitcnt lgkmcnt(1)
	v_smfmac_f32_16x16x64_f16 v[192:195], v[208:211], v[6:13], v191
	ds_read_b128 v[216:219], v141
	s_waitcnt lgkmcnt(1)
	v_smfmac_f32_16x16x64_f16 v[192:195], v[212:215], v[14:21], v191
	ds_read_b128 v[220:223], v142
	s_waitcnt lgkmcnt(1)
	v_smfmac_f32_16x16x64_f16 v[192:195], v[216:219], v[26:33], v191
	s_waitcnt lgkmcnt(0)
	v_smfmac_f32_16x16x64_f16 v[192:195], v[220:223], v[34:41], v191
	s_nop 7
	v_cndmask_b32_e64 v152, v192, v193, s[0:1]
	v_exp_f32_e64 v158, -|v152|
	v_max_f32 v159, 0, v152
	v_add_f32 v158, 1.0, v158
	v_log_f32 v158, v158
	s_nop 0
	v_fma_mixlo_f16 v153, v158, 1.0, v159
	ds_write_b16 v149, v153
	v_mov_b32_e32 v200, v114
	v_mov_b32_e32 v201, v118
	v_mov_b32_e32 v204, v122
	v_mov_b32_e32 v205, v126
	s_nop 1
	ds_read_b128 v[208:211], v143
	s_waitcnt lgkmcnt(1)
	s_barrier
	ds_read_b128 v[212:215], v144
	s_waitcnt lgkmcnt(1)
	v_smfmac_f32_16x16x64_f16 v[200:203], v[208:211], v[42:49], v191
	ds_read_b128 v[216:219], v145
	v_smfmac_f32_16x16x64_f16 v[204:207], v[208:211], v[74:81], v191
	ds_read_b128 v[220:223], v146
	s_waitcnt lgkmcnt(2)
	v_smfmac_f32_16x16x64_f16 v[200:203], v[212:215], v[50:57], v191
	v_smfmac_f32_16x16x64_f16 v[204:207], v[212:215], v[82:89], v191
	s_waitcnt lgkmcnt(1)
	v_smfmac_f32_16x16x64_f16 v[200:203], v[216:219], v[58:65], v191
	v_smfmac_f32_16x16x64_f16 v[204:207], v[216:219], v[90:97], v191
	s_waitcnt lgkmcnt(0)
	v_smfmac_f32_16x16x64_f16 v[200:203], v[220:223], v[66:73], v191
	v_smfmac_f32_16x16x64_f16 v[204:207], v[220:223], v[98:105], v191
	s_nop 6
	v_cndmask_b32_e64 v152, v201, v200, s[6:7]
	v_cndmask_b32_e64 v152, v152, v204, s[0:1]
	v_cndmask_b32_e64 v152, v152, v205, s[4:5]
	v_exp_f32_e32 v152, v152
	s_nop 0
	v_add_f32_e32 v152, 1.0, v152
	v_rcp_f32_e32 v152, v152
	s_nop 0
	v_fmac_f32_e32 v135, v152, v137
	s_nop 1
	v_add_f32_dpp v135, v135, v135 quad_perm:[1,0,3,2] row_mask:0xf bank_mask:0xf bound_ctrl:1
	s_nop 1
	v_add_f32_dpp v135, v135, v135 quad_perm:[2,3,0,1] row_mask:0xf bank_mask:0xf bound_ctrl:1
	s_nop 1
	v_add_f32_dpp v135, v135, v135 row_half_mirror row_mask:0xf bank_mask:0xf bound_ctrl:1
	v_cvt_f16_f32_e32 v137, v135
	ds_write_b16 v150, v137
	s_waitcnt lgkmcnt(0)
	s_barrier
	ds_read_b128 v[158:161], v147
	s_nop 3
	ds_read_b32 v137, v134 offset:32
	v_add_f32_e32 v135, v136, v135
	s_waitcnt lgkmcnt(1)
	v_smfmac_f32_16x16x64_f16 v[130:133], v[158:161], v[248:255], v191
	s_nop 7
	v_cndmask_b32_e64 v156, v130, v131, s[0:1]
	v_exp_f32_e64 v158, -|v156|
	v_max_f32 v159, 0, v156
	v_add_f32 v158, 1.0, v158
	v_log_f32 v158, v158
	s_nop 0
	v_fma_mixlo_f16 v157, v158, 1.0, v159
	ds_write_b16 v148, v157
	v_mov_b32_e32 v192, v106
	v_mov_b32_e32 v193, v110
	v_mul_f32 v136, -2.0, v137
	s_nop 6
	ds_read_b128 v[208:211], v139
	s_waitcnt lgkmcnt(1)
	s_barrier
	ds_read_b128 v[212:215], v140
	s_waitcnt lgkmcnt(1)
	v_smfmac_f32_16x16x64_f16 v[192:195], v[208:211], v[6:13], v191
	ds_read_b128 v[216:219], v141
	s_waitcnt lgkmcnt(1)
	v_smfmac_f32_16x16x64_f16 v[192:195], v[212:215], v[14:21], v191
	ds_read_b128 v[220:223], v142
	s_waitcnt lgkmcnt(1)
	v_smfmac_f32_16x16x64_f16 v[192:195], v[216:219], v[26:33], v191
	s_waitcnt lgkmcnt(0)
	v_smfmac_f32_16x16x64_f16 v[192:195], v[220:223], v[34:41], v191
	s_nop 7
	v_cndmask_b32_e64 v156, v192, v193, s[0:1]
	v_exp_f32_e64 v158, -|v156|
	v_max_f32 v159, 0, v156
	v_add_f32 v158, 1.0, v158
	v_log_f32 v158, v158
	s_nop 0
	v_fma_mixlo_f16 v157, v158, 1.0, v159
	ds_write_b16 v149, v157
	v_mov_b32_e32 v200, v114
	v_mov_b32_e32 v201, v118
	v_mov_b32_e32 v204, v122
	v_mov_b32_e32 v205, v126
	s_nop 1
	ds_read_b128 v[208:211], v143
	s_waitcnt lgkmcnt(1)
	s_barrier
	ds_read_b128 v[212:215], v144
	s_waitcnt lgkmcnt(1)
	v_smfmac_f32_16x16x64_f16 v[200:203], v[208:211], v[42:49], v191
	ds_read_b128 v[216:219], v145
	v_smfmac_f32_16x16x64_f16 v[204:207], v[208:211], v[74:81], v191
	ds_read_b128 v[220:223], v146
	s_waitcnt lgkmcnt(2)
	v_smfmac_f32_16x16x64_f16 v[200:203], v[212:215], v[50:57], v191
	v_smfmac_f32_16x16x64_f16 v[204:207], v[212:215], v[82:89], v191
	s_waitcnt lgkmcnt(1)
	v_smfmac_f32_16x16x64_f16 v[200:203], v[216:219], v[58:65], v191
	v_smfmac_f32_16x16x64_f16 v[204:207], v[216:219], v[90:97], v191
	s_waitcnt lgkmcnt(0)
	v_smfmac_f32_16x16x64_f16 v[200:203], v[220:223], v[66:73], v191
	v_smfmac_f32_16x16x64_f16 v[204:207], v[220:223], v[98:105], v191
	s_nop 6
	v_cndmask_b32_e64 v172, v201, v200, s[6:7]
	v_cndmask_b32_e64 v172, v172, v204, s[0:1]
	v_cndmask_b32_e64 v172, v172, v205, s[4:5]
	v_exp_f32_e32 v172, v172
	s_nop 0
	v_add_f32_e32 v172, 1.0, v172
	v_rcp_f32_e32 v172, v172
	s_nop 0
	v_fmac_f32_e32 v137, v172, v136
	s_nop 1
	v_add_f32_dpp v136, v137, v137 quad_perm:[1,0,3,2] row_mask:0xf bank_mask:0xf bound_ctrl:1
	s_nop 1
	v_add_f32_dpp v136, v136, v136 quad_perm:[2,3,0,1] row_mask:0xf bank_mask:0xf bound_ctrl:1
	s_nop 1
	v_add_f32_dpp v136, v136, v136 row_half_mirror row_mask:0xf bank_mask:0xf bound_ctrl:1
	v_cvt_f16_f32_e32 v137, v136
	ds_write_b16 v150, v137
	s_waitcnt lgkmcnt(0)
	s_barrier
	ds_read_b128 v[156:159], v147
	s_nop 3
	ds_read_b32 v137, v134 offset:64
	v_add_f32_e32 v135, v135, v136
	s_waitcnt lgkmcnt(1)
	v_smfmac_f32_16x16x64_f16 v[130:133], v[156:159], v[248:255], v191
	s_nop 7
	v_cndmask_b32_e64 v156, v130, v131, s[0:1]
	v_exp_f32_e64 v158, -|v156|
	v_max_f32 v159, 0, v156
	v_add_f32 v158, 1.0, v158
	v_log_f32 v158, v158
	s_nop 0
	v_fma_mixlo_f16 v157, v158, 1.0, v159
	ds_write_b16 v148, v157
	v_mov_b32_e32 v192, v106
	v_mov_b32_e32 v193, v110
	v_mul_f32 v136, -2.0, v137
	s_nop 6
	ds_read_b128 v[208:211], v139
	s_waitcnt lgkmcnt(1)
	s_barrier
	ds_read_b128 v[212:215], v140
	s_waitcnt lgkmcnt(1)
	v_smfmac_f32_16x16x64_f16 v[192:195], v[208:211], v[6:13], v191
	ds_read_b128 v[216:219], v141
	s_waitcnt lgkmcnt(1)
	v_smfmac_f32_16x16x64_f16 v[192:195], v[212:215], v[14:21], v191
	ds_read_b128 v[220:223], v142
	s_waitcnt lgkmcnt(1)
	v_smfmac_f32_16x16x64_f16 v[192:195], v[216:219], v[26:33], v191
	s_waitcnt lgkmcnt(0)
	v_smfmac_f32_16x16x64_f16 v[192:195], v[220:223], v[34:41], v191
	s_nop 7
	v_cndmask_b32_e64 v156, v192, v193, s[0:1]
	v_exp_f32_e64 v158, -|v156|
	v_max_f32 v159, 0, v156
	v_add_f32 v158, 1.0, v158
	v_log_f32 v158, v158
	s_nop 0
	v_fma_mixlo_f16 v157, v158, 1.0, v159
	ds_write_b16 v149, v157
	v_mov_b32_e32 v200, v114
	v_mov_b32_e32 v201, v118
	v_mov_b32_e32 v204, v122
	v_mov_b32_e32 v205, v126
	s_nop 1
	ds_read_b128 v[208:211], v143
	s_waitcnt lgkmcnt(1)
	s_barrier
	ds_read_b128 v[212:215], v144
	s_waitcnt lgkmcnt(1)
	v_smfmac_f32_16x16x64_f16 v[200:203], v[208:211], v[42:49], v191
	ds_read_b128 v[216:219], v145
	v_smfmac_f32_16x16x64_f16 v[204:207], v[208:211], v[74:81], v191
	ds_read_b128 v[220:223], v146
	s_waitcnt lgkmcnt(2)
	v_smfmac_f32_16x16x64_f16 v[200:203], v[212:215], v[50:57], v191
	v_smfmac_f32_16x16x64_f16 v[204:207], v[212:215], v[82:89], v191
	s_waitcnt lgkmcnt(1)
	v_smfmac_f32_16x16x64_f16 v[200:203], v[216:219], v[58:65], v191
	v_smfmac_f32_16x16x64_f16 v[204:207], v[216:219], v[90:97], v191
	s_waitcnt lgkmcnt(0)
	v_smfmac_f32_16x16x64_f16 v[200:203], v[220:223], v[66:73], v191
	v_smfmac_f32_16x16x64_f16 v[204:207], v[220:223], v[98:105], v191
	s_nop 6
	v_cndmask_b32_e64 v172, v201, v200, s[6:7]
	v_cndmask_b32_e64 v172, v172, v204, s[0:1]
	v_cndmask_b32_e64 v172, v172, v205, s[4:5]
	v_exp_f32_e32 v172, v172
	s_nop 0
	v_add_f32_e32 v172, 1.0, v172
	v_rcp_f32_e32 v172, v172
	s_nop 0
	v_fmac_f32_e32 v137, v172, v136
	s_nop 1
	v_add_f32_dpp v136, v137, v137 quad_perm:[1,0,3,2] row_mask:0xf bank_mask:0xf bound_ctrl:1
	s_nop 1
	v_add_f32_dpp v136, v136, v136 quad_perm:[2,3,0,1] row_mask:0xf bank_mask:0xf bound_ctrl:1
	s_nop 1
	v_add_f32_dpp v136, v136, v136 row_half_mirror row_mask:0xf bank_mask:0xf bound_ctrl:1
	v_cvt_f16_f32_e32 v137, v136
	ds_write_b16 v150, v137
	s_waitcnt lgkmcnt(0)
	s_barrier
	ds_read_b128 v[156:159], v147
	s_nop 3
	ds_read_b32 v137, v134 offset:96
	v_add_f32_e32 v135, v135, v136
	s_waitcnt lgkmcnt(1)
	v_smfmac_f32_16x16x64_f16 v[130:133], v[156:159], v[248:255], v191
	s_nop 7
	v_cndmask_b32_e64 v156, v130, v131, s[0:1]
	v_exp_f32_e64 v158, -|v156|
	v_max_f32 v159, 0, v156
	v_add_f32 v158, 1.0, v158
	v_log_f32 v158, v158
	s_nop 0
	v_fma_mixlo_f16 v157, v158, 1.0, v159
	ds_write_b16 v148, v157
	v_mov_b32_e32 v192, v106
	v_mov_b32_e32 v193, v110
	v_mul_f32 v136, -2.0, v137
	s_nop 6
	ds_read_b128 v[208:211], v139
	s_waitcnt lgkmcnt(1)
	s_barrier
	ds_read_b128 v[212:215], v140
	s_waitcnt lgkmcnt(1)
	v_smfmac_f32_16x16x64_f16 v[192:195], v[208:211], v[6:13], v191
	ds_read_b128 v[216:219], v141
	s_waitcnt lgkmcnt(1)
	v_smfmac_f32_16x16x64_f16 v[192:195], v[212:215], v[14:21], v191
	ds_read_b128 v[220:223], v142
	s_waitcnt lgkmcnt(1)
	v_smfmac_f32_16x16x64_f16 v[192:195], v[216:219], v[26:33], v191
	s_waitcnt lgkmcnt(0)
	v_smfmac_f32_16x16x64_f16 v[192:195], v[220:223], v[34:41], v191
	s_nop 7
	v_cndmask_b32_e64 v156, v192, v193, s[0:1]
	v_exp_f32_e64 v158, -|v156|
	v_max_f32 v159, 0, v156
	v_add_f32 v158, 1.0, v158
	v_log_f32 v158, v158
	s_nop 0
	v_fma_mixlo_f16 v157, v158, 1.0, v159
	ds_write_b16 v149, v157
	v_mov_b32_e32 v200, v114
	v_mov_b32_e32 v201, v118
	v_mov_b32_e32 v204, v122
	v_mov_b32_e32 v205, v126
	s_nop 1
	ds_read_b128 v[208:211], v143
	s_waitcnt lgkmcnt(1)
	s_barrier
	ds_read_b128 v[212:215], v144
	s_waitcnt lgkmcnt(1)
	v_smfmac_f32_16x16x64_f16 v[200:203], v[208:211], v[42:49], v191
	ds_read_b128 v[216:219], v145
	v_smfmac_f32_16x16x64_f16 v[204:207], v[208:211], v[74:81], v191
	ds_read_b128 v[220:223], v146
	s_waitcnt lgkmcnt(2)
	v_smfmac_f32_16x16x64_f16 v[200:203], v[212:215], v[50:57], v191
	v_smfmac_f32_16x16x64_f16 v[204:207], v[212:215], v[82:89], v191
	s_waitcnt lgkmcnt(1)
	v_smfmac_f32_16x16x64_f16 v[200:203], v[216:219], v[58:65], v191
	v_smfmac_f32_16x16x64_f16 v[204:207], v[216:219], v[90:97], v191
	s_waitcnt lgkmcnt(0)
	v_smfmac_f32_16x16x64_f16 v[200:203], v[220:223], v[66:73], v191
	v_smfmac_f32_16x16x64_f16 v[204:207], v[220:223], v[98:105], v191
	s_nop 6
	v_cndmask_b32_e64 v172, v201, v200, s[6:7]
	v_cndmask_b32_e64 v172, v172, v204, s[0:1]
	v_cndmask_b32_e64 v172, v172, v205, s[4:5]
	v_exp_f32_e32 v172, v172
	s_nop 0
	v_add_f32_e32 v172, 1.0, v172
	v_rcp_f32_e32 v172, v172
	s_nop 0
	v_fmac_f32_e32 v137, v172, v136
	s_nop 1
	v_add_f32_dpp v136, v137, v137 quad_perm:[1,0,3,2] row_mask:0xf bank_mask:0xf bound_ctrl:1
	s_nop 1
	v_add_f32_dpp v136, v136, v136 quad_perm:[2,3,0,1] row_mask:0xf bank_mask:0xf bound_ctrl:1
	s_nop 1
	v_add_f32_dpp v136, v136, v136 row_half_mirror row_mask:0xf bank_mask:0xf bound_ctrl:1
	v_cvt_f16_f32_e32 v137, v136
	ds_write_b16 v150, v137
	s_waitcnt lgkmcnt(0)
	s_barrier
	ds_read_b128 v[156:159], v147
	s_nop 3
	ds_read_b32 v137, v134 offset:128
	v_add_f32_e32 v135, v135, v136
	s_waitcnt lgkmcnt(1)
	v_smfmac_f32_16x16x64_f16 v[130:133], v[156:159], v[248:255], v191
	s_nop 7
	v_cndmask_b32_e64 v156, v130, v131, s[0:1]
	v_exp_f32_e64 v158, -|v156|
	v_max_f32 v159, 0, v156
	v_add_f32 v158, 1.0, v158
	v_log_f32 v158, v158
	s_nop 0
	v_fma_mixlo_f16 v157, v158, 1.0, v159
	ds_write_b16 v148, v157
	v_mov_b32_e32 v192, v106
	v_mov_b32_e32 v193, v110
	v_mul_f32 v136, -2.0, v137
	s_nop 6
	ds_read_b128 v[208:211], v139
	s_waitcnt lgkmcnt(1)
	s_barrier
	ds_read_b128 v[212:215], v140
	s_waitcnt lgkmcnt(1)
	v_smfmac_f32_16x16x64_f16 v[192:195], v[208:211], v[6:13], v191
	ds_read_b128 v[216:219], v141
	s_waitcnt lgkmcnt(1)
	v_smfmac_f32_16x16x64_f16 v[192:195], v[212:215], v[14:21], v191
	ds_read_b128 v[220:223], v142
	s_waitcnt lgkmcnt(1)
	v_smfmac_f32_16x16x64_f16 v[192:195], v[216:219], v[26:33], v191
	s_waitcnt lgkmcnt(0)
	v_smfmac_f32_16x16x64_f16 v[192:195], v[220:223], v[34:41], v191
	s_nop 7
	v_cndmask_b32_e64 v156, v192, v193, s[0:1]
	v_exp_f32_e64 v158, -|v156|
	v_max_f32 v159, 0, v156
	v_add_f32 v158, 1.0, v158
	v_log_f32 v158, v158
	s_nop 0
	v_fma_mixlo_f16 v157, v158, 1.0, v159
	ds_write_b16 v149, v157
	v_mov_b32_e32 v200, v114
	v_mov_b32_e32 v201, v118
	v_mov_b32_e32 v204, v122
	v_mov_b32_e32 v205, v126
	s_nop 1
	ds_read_b128 v[208:211], v143
	s_waitcnt lgkmcnt(1)
	s_barrier
	ds_read_b128 v[212:215], v144
	s_waitcnt lgkmcnt(1)
	v_smfmac_f32_16x16x64_f16 v[200:203], v[208:211], v[42:49], v191
	ds_read_b128 v[216:219], v145
	v_smfmac_f32_16x16x64_f16 v[204:207], v[208:211], v[74:81], v191
	ds_read_b128 v[220:223], v146
	s_waitcnt lgkmcnt(2)
	v_smfmac_f32_16x16x64_f16 v[200:203], v[212:215], v[50:57], v191
	v_smfmac_f32_16x16x64_f16 v[204:207], v[212:215], v[82:89], v191
	s_waitcnt lgkmcnt(1)
	v_smfmac_f32_16x16x64_f16 v[200:203], v[216:219], v[58:65], v191
	v_smfmac_f32_16x16x64_f16 v[204:207], v[216:219], v[90:97], v191
	s_waitcnt lgkmcnt(0)
	v_smfmac_f32_16x16x64_f16 v[200:203], v[220:223], v[66:73], v191
	v_smfmac_f32_16x16x64_f16 v[204:207], v[220:223], v[98:105], v191
	s_nop 6
	v_cndmask_b32_e64 v172, v201, v200, s[6:7]
	v_cndmask_b32_e64 v172, v172, v204, s[0:1]
	v_cndmask_b32_e64 v172, v172, v205, s[4:5]
	v_exp_f32_e32 v172, v172
	s_nop 0
	v_add_f32_e32 v172, 1.0, v172
	v_rcp_f32_e32 v172, v172
	s_nop 0
	v_fmac_f32_e32 v137, v172, v136
	s_nop 1
	v_add_f32_dpp v136, v137, v137 quad_perm:[1,0,3,2] row_mask:0xf bank_mask:0xf bound_ctrl:1
	s_nop 1
	v_add_f32_dpp v136, v136, v136 quad_perm:[2,3,0,1] row_mask:0xf bank_mask:0xf bound_ctrl:1
	s_nop 1
	v_add_f32_dpp v136, v136, v136 row_half_mirror row_mask:0xf bank_mask:0xf bound_ctrl:1
	v_cvt_f16_f32_e32 v137, v136
	ds_write_b16 v150, v137
	s_waitcnt lgkmcnt(0)
	s_barrier
	ds_read_b128 v[156:159], v147
	s_nop 3
	ds_read_b32 v137, v134 offset:160
	v_add_f32_e32 v135, v135, v136
	s_waitcnt lgkmcnt(1)
	v_smfmac_f32_16x16x64_f16 v[130:133], v[156:159], v[248:255], v191
	s_nop 7
	v_cndmask_b32_e64 v156, v130, v131, s[0:1]
	v_exp_f32_e64 v158, -|v156|
	v_max_f32 v159, 0, v156
	v_add_f32 v158, 1.0, v158
	v_log_f32 v158, v158
	s_nop 0
	v_fma_mixlo_f16 v157, v158, 1.0, v159
	ds_write_b16 v148, v157
	v_mov_b32_e32 v192, v106
	v_mov_b32_e32 v193, v110
	v_mul_f32 v136, -2.0, v137
	s_nop 6
	ds_read_b128 v[208:211], v139
	s_waitcnt lgkmcnt(1)
	s_barrier
	ds_read_b128 v[212:215], v140
	s_waitcnt lgkmcnt(1)
	v_smfmac_f32_16x16x64_f16 v[192:195], v[208:211], v[6:13], v191
	ds_read_b128 v[216:219], v141
	s_waitcnt lgkmcnt(1)
	v_smfmac_f32_16x16x64_f16 v[192:195], v[212:215], v[14:21], v191
	ds_read_b128 v[220:223], v142
	s_waitcnt lgkmcnt(1)
	v_smfmac_f32_16x16x64_f16 v[192:195], v[216:219], v[26:33], v191
	s_waitcnt lgkmcnt(0)
	v_smfmac_f32_16x16x64_f16 v[192:195], v[220:223], v[34:41], v191
	s_nop 7
	v_cndmask_b32_e64 v156, v192, v193, s[0:1]
	v_exp_f32_e64 v158, -|v156|
	v_max_f32 v159, 0, v156
	v_add_f32 v158, 1.0, v158
	v_log_f32 v158, v158
	s_nop 0
	v_fma_mixlo_f16 v157, v158, 1.0, v159
	ds_write_b16 v149, v157
	v_mov_b32_e32 v200, v114
	v_mov_b32_e32 v201, v118
	v_mov_b32_e32 v204, v122
	v_mov_b32_e32 v205, v126
	s_nop 1
	ds_read_b128 v[208:211], v143
	s_waitcnt lgkmcnt(1)
	s_barrier
	ds_read_b128 v[212:215], v144
	s_waitcnt lgkmcnt(1)
	v_smfmac_f32_16x16x64_f16 v[200:203], v[208:211], v[42:49], v191
	ds_read_b128 v[216:219], v145
	v_smfmac_f32_16x16x64_f16 v[204:207], v[208:211], v[74:81], v191
	ds_read_b128 v[220:223], v146
	s_waitcnt lgkmcnt(2)
	v_smfmac_f32_16x16x64_f16 v[200:203], v[212:215], v[50:57], v191
	v_smfmac_f32_16x16x64_f16 v[204:207], v[212:215], v[82:89], v191
	s_waitcnt lgkmcnt(1)
	v_smfmac_f32_16x16x64_f16 v[200:203], v[216:219], v[58:65], v191
	v_smfmac_f32_16x16x64_f16 v[204:207], v[216:219], v[90:97], v191
	s_waitcnt lgkmcnt(0)
	v_smfmac_f32_16x16x64_f16 v[200:203], v[220:223], v[66:73], v191
	v_smfmac_f32_16x16x64_f16 v[204:207], v[220:223], v[98:105], v191
	s_nop 6
	v_cndmask_b32_e64 v172, v201, v200, s[6:7]
	v_cndmask_b32_e64 v172, v172, v204, s[0:1]
	v_cndmask_b32_e64 v172, v172, v205, s[4:5]
	v_exp_f32_e32 v172, v172
	s_nop 0
	v_add_f32_e32 v172, 1.0, v172
	v_rcp_f32_e32 v172, v172
	s_nop 0
	v_fmac_f32_e32 v137, v172, v136
	s_nop 1
	v_add_f32_dpp v136, v137, v137 quad_perm:[1,0,3,2] row_mask:0xf bank_mask:0xf bound_ctrl:1
	s_nop 1
	v_add_f32_dpp v136, v136, v136 quad_perm:[2,3,0,1] row_mask:0xf bank_mask:0xf bound_ctrl:1
	s_nop 1
	v_add_f32_dpp v136, v136, v136 row_half_mirror row_mask:0xf bank_mask:0xf bound_ctrl:1
	v_cvt_f16_f32_e32 v137, v136
	ds_write_b16 v150, v137
	s_waitcnt lgkmcnt(0)
	s_barrier
	ds_read_b128 v[156:159], v147
	s_nop 3
	ds_read_b32 v137, v134 offset:192
	v_add_f32_e32 v135, v135, v136
	s_waitcnt lgkmcnt(1)
	v_smfmac_f32_16x16x64_f16 v[130:133], v[156:159], v[248:255], v191
	s_nop 7
	v_cndmask_b32_e64 v152, v130, v131, s[0:1]
	v_exp_f32_e64 v158, -|v152|
	v_max_f32 v159, 0, v152
	v_add_f32 v158, 1.0, v158
	v_log_f32 v158, v158
	s_nop 0
	v_fma_mixlo_f16 v153, v158, 1.0, v159
	ds_write_b16 v148, v153
	v_mov_b32_e32 v192, v106
	v_mov_b32_e32 v193, v110
	v_mul_f32 v136, -2.0, v137
	s_nop 6
	ds_read_b128 v[208:211], v139
	s_waitcnt lgkmcnt(1)
	s_barrier
	ds_read_b128 v[212:215], v140
	s_waitcnt lgkmcnt(1)
	v_smfmac_f32_16x16x64_f16 v[192:195], v[208:211], v[6:13], v191
	ds_read_b128 v[216:219], v141
	s_waitcnt lgkmcnt(1)
	v_smfmac_f32_16x16x64_f16 v[192:195], v[212:215], v[14:21], v191
	ds_read_b128 v[220:223], v142
	s_waitcnt lgkmcnt(1)
	v_smfmac_f32_16x16x64_f16 v[192:195], v[216:219], v[26:33], v191
	s_waitcnt lgkmcnt(0)
	v_smfmac_f32_16x16x64_f16 v[192:195], v[220:223], v[34:41], v191
	s_nop 7
	v_cndmask_b32_e64 v152, v192, v193, s[0:1]
	v_exp_f32_e64 v158, -|v152|
	v_max_f32 v159, 0, v152
	v_add_f32 v158, 1.0, v158
	v_log_f32 v158, v158
	s_nop 0
	v_fma_mixlo_f16 v153, v158, 1.0, v159
	ds_write_b16 v149, v153
	v_mov_b32_e32 v200, v114
	v_mov_b32_e32 v201, v118
	v_mov_b32_e32 v204, v122
	v_mov_b32_e32 v205, v126
	s_nop 1
	ds_read_b128 v[208:211], v143
	s_waitcnt lgkmcnt(1)
	s_barrier
	ds_read_b128 v[212:215], v144
	s_waitcnt lgkmcnt(1)
	v_smfmac_f32_16x16x64_f16 v[200:203], v[208:211], v[42:49], v191
	ds_read_b128 v[216:219], v145
	v_smfmac_f32_16x16x64_f16 v[204:207], v[208:211], v[74:81], v191
	ds_read_b128 v[220:223], v146
	s_waitcnt lgkmcnt(2)
	v_smfmac_f32_16x16x64_f16 v[200:203], v[212:215], v[50:57], v191
	v_smfmac_f32_16x16x64_f16 v[204:207], v[212:215], v[82:89], v191
	s_waitcnt lgkmcnt(1)
	v_smfmac_f32_16x16x64_f16 v[200:203], v[216:219], v[58:65], v191
	v_smfmac_f32_16x16x64_f16 v[204:207], v[216:219], v[90:97], v191
	s_waitcnt lgkmcnt(0)
	v_smfmac_f32_16x16x64_f16 v[200:203], v[220:223], v[66:73], v191
	v_smfmac_f32_16x16x64_f16 v[204:207], v[220:223], v[98:105], v191
	s_nop 6
	v_cndmask_b32_e64 v152, v201, v200, s[6:7]
	v_cndmask_b32_e64 v152, v152, v204, s[0:1]
	v_cndmask_b32_e64 v152, v152, v205, s[4:5]
	v_exp_f32_e32 v152, v152
	s_nop 0
	v_add_f32_e32 v152, 1.0, v152
	v_rcp_f32_e32 v152, v152
	s_nop 0
	v_fmac_f32_e32 v137, v152, v136
	s_nop 1
	v_add_f32_dpp v136, v137, v137 quad_perm:[1,0,3,2] row_mask:0xf bank_mask:0xf bound_ctrl:1
	s_nop 1
	v_add_f32_dpp v136, v136, v136 quad_perm:[2,3,0,1] row_mask:0xf bank_mask:0xf bound_ctrl:1
	s_nop 1
	v_add_f32_dpp v136, v136, v136 row_half_mirror row_mask:0xf bank_mask:0xf bound_ctrl:1
	v_cvt_f16_f32_e32 v137, v136
	ds_write_b16 v150, v137
	s_waitcnt lgkmcnt(0)
	s_barrier
	ds_read_b128 v[158:161], v147
	v_add_f32_e32 v152, v135, v136
	ds_read_b32 v153, v134 offset:224
	s_addk_i32 s3, 0x100
	s_cmpk_eq_u32 s3, 0xfa20
	s_waitcnt lgkmcnt(1)
	v_smfmac_f32_16x16x64_f16 v[130:133], v[158:161], v[248:255], v191
	s_nop 7
	v_cndmask_b32_e64 v154, v130, v131, s[0:1]
	s_cbranch_scc0 .LBB0_21
	s_and_saveexec_b64 s[0:1], vcc
	ds_write_b32 v1, v152
	s_or_b64 exec, exec, s[0:1]
	v_cmp_gt_u32_e32 vcc, 10, v0
	s_waitcnt lgkmcnt(0)
	s_barrier
	s_and_saveexec_b64 s[0:1], vcc
	s_cbranch_execz .LBB0_28
	v_lshlrev_b32_e32 v1, 2, v0
	global_load_dword v1, v1, s[12:13]
	v_mov_b32_e32 v139, 0
	v_lshl_add_u64 v[2:3], s[10:11], 0, v[138:139]
	v_lshl_add_u64 v[2:3], v[2:3], 0, 28
	s_mov_b32 s0, 0
